# v19 + bucketsort run len/lo LDS reads hoisted ahead of the chunk loads
# baseline (speedup 1.0000x reference)
.LBB2_2:
	s_or_b64 exec, exec, s[4:5]
	s_movk_i32 s3, 0x300
	v_cmp_gt_u32_e32 vcc, s3, v0
	s_and_saveexec_b64 s[4:5], vcc
	v_lshlrev_b32_e32 v1, 2, v0
	v_mov_b32_e32 v2, 0
	ds_write_b32 v1, v2 offset:49152
	s_or_b64 exec, exec, s[4:5]
	s_load_dwordx4 s[56:59], s[0:1], 0x0
	s_load_dwordx4 s[52:55], s[0:1], 0x18
	v_mbcnt_lo_u32_b32 v1, -1, 0
	v_mbcnt_hi_u32_b32 v1, -1, v1
	v_and_b32_e32 v2, 63, v0
	v_add_u32_dpp v4, v4, v4 quad_perm:[1,0,3,2] row_mask:0xf bank_mask:0xf
	v_add_u32_dpp v5, v5, v5 quad_perm:[1,0,3,2] row_mask:0xf bank_mask:0xf
	v_cmp_eq_u32_e64 s[46:47], 0, v2
	v_cmp_gt_u32_e64 s[4:5], 2, v2
	v_add_u32_dpp v4, v4, v4 quad_perm:[2,3,0,1] row_mask:0xf bank_mask:0xf
	v_add_u32_dpp v5, v5, v5 quad_perm:[2,3,0,1] row_mask:0xf bank_mask:0xf
	v_cmp_gt_u32_e64 s[8:9], 4, v2
	v_cmp_gt_u32_e64 s[6:7], 8, v2
	v_add_u32_dpp v4, v4, v4 row_half_mirror row_mask:0xf bank_mask:0xf
	v_add_u32_dpp v5, v5, v5 row_half_mirror row_mask:0xf bank_mask:0xf
	v_cmp_gt_u32_e64 s[10:11], 16, v2
	v_cmp_gt_u32_e64 s[18:19], 32, v2
	v_add_u32_dpp v4, v4, v4 row_mirror row_mask:0xf bank_mask:0xf
	v_add_u32_dpp v5, v5, v5 row_mirror row_mask:0xf bank_mask:0xf
	v_cmp_eq_u32_e64 s[14:15], 63, v2
	v_add_u32_e32 v3, -1, v1
	v_cndmask_b32_e64 v3, v3, v1, s[46:47]
	v_lshlrev_b32_e32 v3, 2, v3
	v_readlane_b32 s20, v4, 0
	v_readlane_b32 s21, v4, 16
	v_readlane_b32 s22, v4, 32
	v_readlane_b32 s23, v4, 48
	v_readlane_b32 s24, v5, 0
	v_readlane_b32 s25, v5, 16
	v_readlane_b32 s26, v5, 32
	v_readlane_b32 s27, v5, 48
	v_add_u32_e32 v6, -2, v1
	v_cndmask_b32_e64 v6, v6, v1, s[4:5]
	v_lshlrev_b32_e32 v6, 2, v6
	v_add_u32_e32 v7, -4, v1
	v_cndmask_b32_e64 v7, v7, v1, s[8:9]
	v_lshlrev_b32_e32 v7, 2, v7
	v_add_u32_e32 v40, -8, v1
	v_cndmask_b32_e64 v40, v40, v1, s[6:7]
	v_lshlrev_b32_e32 v40, 2, v40
	v_add_u32_e32 v43, -16, v1
	v_cndmask_b32_e64 v43, v43, v1, s[10:11]
	v_lshlrev_b32_e32 v43, 2, v43
	v_subrev_u32_e32 v44, 32, v1
	v_cndmask_b32_e64 v44, v44, v1, s[18:19]
	v_lshlrev_b32_e32 v44, 2, v44
	s_add_i32 s20, s20, s21
	s_add_i32 s22, s22, s23
	s_add_i32 s20, s20, s22
	s_add_i32 s24, s24, s25
	s_add_i32 s26, s26, s27
	s_add_i32 s24, s24, s26
	v_lshrrev_b32_e32 v1, 6, v0
	v_lshlrev_b32_e32 v8, 2, v1
	v_lshlrev_b32_e32 v9, 3, v1
	v_mov_b32_e32 v10, s20
	v_mov_b32_e32 v11, s24
	s_and_saveexec_b64 s[18:19], s[46:47]
	ds_write_b64 v9, v[10:11] offset:54016
	s_mov_b64 exec, s[18:19]
	v_cmp_lt_u32_e64 s[12:13], 63, v0
	v_cmp_gt_u32_e64 s[16:17], 64, v0
	v_mov_b32_e32 v39, 0
	s_waitcnt lgkmcnt(0)
	s_barrier
	ds_read_b128 v[10:13], v39 offset:54016
	ds_read_b128 v[14:17], v39 offset:54032
	s_waitcnt lgkmcnt(0)
	v_add_u32_e32 v4, v10, v12
	v_add_u32_e32 v5, v11, v13
	v_add3_u32 v4, v4, v14, v16
	v_add3_u32 v5, v5, v15, v17
	s_nop 0
	v_readfirstlane_b32 s50, v4
	v_readfirstlane_b32 s33, v5
	ds_read_b32 v53, v8 offset:53120
	v_or_b32_e32 v9, 0xcf80, v8
	ds_read_b32 v52, v9 offset:64
	ds_read_b32 v51, v9 offset:128
	ds_read_b32 v50, v9 offset:192
	ds_read_b32 v49, v9 offset:256
	ds_read_b32 v48, v9 offset:320
	ds_read_b32 v45, v9 offset:384
	ds_read_b32 v42, v9 offset:448
	ds_read_b32 v38, v9 offset:512
	ds_read_b32 v35, v9 offset:576
	ds_read_b32 v33, v9 offset:640
	ds_read_b32 v31, v9 offset:704
	ds_read_b32 v55, v9 offset:768
	ds_read_b32 v54, v8 offset:52224
	ds_read_b32 v56, v8 offset:52288
	ds_read_b32 v57, v8 offset:52352
	ds_read_b32 v58, v8 offset:52416
	ds_read_b32 v59, v8 offset:52480
	ds_read_b32 v60, v8 offset:52544
	ds_read_b32 v61, v8 offset:52608
	ds_read_b32 v62, v8 offset:52672
	ds_read_b32 v63, v8 offset:52736
	v_mov_b32_e32 v47, 0
	v_mov_b32_e32 v46, 0
	s_waitcnt lgkmcnt(0)
	v_cmp_lt_i32_e64 s[44:45], v2, v53
	s_and_saveexec_b64 s[0:1], s[44:45]
	s_cbranch_execz .LBB2_20
	v_mov_b32_e32 v4, v54
	v_lshl_or_b32 v10, v1, 14, v2
	v_mov_b32_e32 v11, 0
	s_waitcnt lgkmcnt(0)
	v_ashrrev_i32_e32 v5, 31, v4
	v_lshl_add_u64 v[4:5], v[10:11], 0, v[4:5]
	v_lshl_add_u64 v[10:11], v[4:5], 2, s[56:57]
	v_lshl_add_u64 v[4:5], v[4:5], 1, s[58:59]
	global_load_dword v46, v[10:11], off
	global_load_ushort v47, v[4:5], off
.LBB2_20:
	s_or_b64 exec, exec, s[0:1]
	v_lshlrev_b32_e32 v4, 14, v1
	v_mov_b32_e32 v41, 0
	s_waitcnt lgkmcnt(0)
	v_cmp_lt_i32_e64 s[42:43], v2, v52
	s_and_saveexec_b64 s[0:1], s[42:43]
	s_cbranch_execz .LBB2_22
	v_mov_b32_e32 v10, v56
	s_mov_b32 s3, 0x40000
	v_mov_b32_e32 v13, 0
	v_or3_b32 v12, v4, v2, s3
	s_waitcnt lgkmcnt(0)
	v_ashrrev_i32_e32 v11, 31, v10
	v_lshl_add_u64 v[10:11], v[12:13], 0, v[10:11]
	v_lshl_add_u64 v[12:13], v[10:11], 2, s[56:57]
	v_lshl_add_u64 v[10:11], v[10:11], 1, s[58:59]
	global_load_dword v41, v[12:13], off
	global_load_ushort v39, v[10:11], off
.LBB2_22:
	s_or_b64 exec, exec, s[0:1]
	v_mov_b32_e32 v32, 0
	v_mov_b32_e32 v37, 0
	v_mov_b32_e32 v36, 0
	s_waitcnt lgkmcnt(0)
	v_cmp_lt_i32_e64 s[40:41], v2, v51
	s_and_saveexec_b64 s[0:1], s[40:41]
	s_cbranch_execz .LBB2_24
	v_mov_b32_e32 v10, v57
	s_mov_b32 s3, 0x80000
	v_mov_b32_e32 v13, 0
	v_or3_b32 v12, v4, v2, s3
	s_waitcnt lgkmcnt(0)
	v_ashrrev_i32_e32 v11, 31, v10
	v_lshl_add_u64 v[10:11], v[12:13], 0, v[10:11]
	v_lshl_add_u64 v[12:13], v[10:11], 2, s[56:57]
	v_lshl_add_u64 v[10:11], v[10:11], 1, s[58:59]
	global_load_dword v36, v[12:13], off
	global_load_ushort v37, v[10:11], off
.LBB2_24:
	s_or_b64 exec, exec, s[0:1]
	v_mov_b32_e32 v34, 0
	s_waitcnt lgkmcnt(0)
	v_cmp_lt_i32_e64 s[38:39], v2, v50
	s_and_saveexec_b64 s[0:1], s[38:39]
	s_cbranch_execz .LBB2_26
	v_mov_b32_e32 v10, v58
	s_mov_b32 s3, 0xc0000
	v_mov_b32_e32 v13, 0
	v_or3_b32 v12, v4, v2, s3
	s_waitcnt lgkmcnt(0)
	v_ashrrev_i32_e32 v11, 31, v10
	v_lshl_add_u64 v[10:11], v[12:13], 0, v[10:11]
	v_lshl_add_u64 v[12:13], v[10:11], 2, s[56:57]
	v_lshl_add_u64 v[10:11], v[10:11], 1, s[58:59]
	global_load_dword v34, v[12:13], off
	global_load_ushort v32, v[10:11], off
.LBB2_26:
	s_or_b64 exec, exec, s[0:1]
	v_mov_b32_e32 v27, 0
	v_mov_b32_e32 v30, 0
	v_mov_b32_e32 v29, 0
	s_waitcnt lgkmcnt(0)
	v_cmp_lt_i32_e64 s[36:37], v2, v49
	s_and_saveexec_b64 s[0:1], s[36:37]
	s_cbranch_execz .LBB2_28
	v_mov_b32_e32 v10, v59
	s_mov_b32 s3, 0x100000
	v_mov_b32_e32 v13, 0
	v_or3_b32 v12, v4, v2, s3
	s_waitcnt lgkmcnt(0)
	v_ashrrev_i32_e32 v11, 31, v10
	v_lshl_add_u64 v[10:11], v[12:13], 0, v[10:11]
	v_lshl_add_u64 v[12:13], v[10:11], 2, s[56:57]
	v_lshl_add_u64 v[10:11], v[10:11], 1, s[58:59]
	global_load_dword v29, v[12:13], off
	global_load_ushort v30, v[10:11], off
.LBB2_28:
	s_or_b64 exec, exec, s[0:1]
	v_mov_b32_e32 v28, 0
	s_waitcnt lgkmcnt(0)
	v_cmp_lt_i32_e64 s[34:35], v2, v48
	s_and_saveexec_b64 s[0:1], s[34:35]
	s_cbranch_execz .LBB2_30
	v_mov_b32_e32 v10, v60
	s_mov_b32 s3, 0x140000
	v_mov_b32_e32 v13, 0
	v_or3_b32 v12, v4, v2, s3
	s_waitcnt lgkmcnt(0)
	v_ashrrev_i32_e32 v11, 31, v10
	v_lshl_add_u64 v[10:11], v[12:13], 0, v[10:11]
	v_lshl_add_u64 v[12:13], v[10:11], 2, s[56:57]
	v_lshl_add_u64 v[10:11], v[10:11], 1, s[58:59]
	global_load_dword v28, v[12:13], off
	global_load_ushort v27, v[10:11], off
.LBB2_30:
	s_or_b64 exec, exec, s[0:1]
	v_mov_b32_e32 v23, 0
	v_mov_b32_e32 v26, 0
	v_mov_b32_e32 v25, 0
	s_waitcnt lgkmcnt(0)
	v_cmp_lt_i32_e64 s[30:31], v2, v45
	s_and_saveexec_b64 s[0:1], s[30:31]
	s_cbranch_execz .LBB2_32
	v_mov_b32_e32 v10, v61
	s_mov_b32 s3, 0x180000
	v_mov_b32_e32 v13, 0
	v_or3_b32 v12, v4, v2, s3
	s_waitcnt lgkmcnt(0)
	v_ashrrev_i32_e32 v11, 31, v10
	v_lshl_add_u64 v[10:11], v[12:13], 0, v[10:11]
	v_lshl_add_u64 v[12:13], v[10:11], 2, s[56:57]
	v_lshl_add_u64 v[10:11], v[10:11], 1, s[58:59]
	global_load_dword v25, v[12:13], off
	global_load_ushort v26, v[10:11], off
.LBB2_32:
	s_or_b64 exec, exec, s[0:1]
	v_mov_b32_e32 v24, 0
	s_waitcnt lgkmcnt(0)
	v_cmp_lt_i32_e64 s[28:29], v2, v42
	s_and_saveexec_b64 s[0:1], s[28:29]
	s_cbranch_execz .LBB2_34
	v_mov_b32_e32 v10, v62
	s_mov_b32 s3, 0x1c0000
	v_mov_b32_e32 v13, 0
	v_or3_b32 v12, v4, v2, s3
	s_waitcnt lgkmcnt(0)
	v_ashrrev_i32_e32 v11, 31, v10
	v_lshl_add_u64 v[10:11], v[12:13], 0, v[10:11]
	v_lshl_add_u64 v[12:13], v[10:11], 2, s[56:57]
	v_lshl_add_u64 v[10:11], v[10:11], 1, s[58:59]
	global_load_dword v24, v[12:13], off
	global_load_ushort v23, v[10:11], off
.LBB2_34:
	s_or_b64 exec, exec, s[0:1]
	v_mov_b32_e32 v19, 0
	v_mov_b32_e32 v22, 0
	v_mov_b32_e32 v21, 0
	s_waitcnt lgkmcnt(0)
	v_cmp_lt_i32_e64 s[26:27], v2, v38
	s_and_saveexec_b64 s[0:1], s[26:27]
	s_cbranch_execz .LBB2_36
	v_mov_b32_e32 v10, v63
	s_mov_b32 s3, 0x200000
	v_mov_b32_e32 v13, 0
	v_or3_b32 v12, v4, v2, s3
	s_waitcnt lgkmcnt(0)
	v_ashrrev_i32_e32 v11, 31, v10
	v_lshl_add_u64 v[10:11], v[12:13], 0, v[10:11]
	v_lshl_add_u64 v[12:13], v[10:11], 2, s[56:57]
	v_lshl_add_u64 v[10:11], v[10:11], 1, s[58:59]
	global_load_dword v21, v[12:13], off
	global_load_ushort v22, v[10:11], off
.LBB2_36:
	s_or_b64 exec, exec, s[0:1]
	v_mov_b32_e32 v20, 0
	s_waitcnt lgkmcnt(0)
	v_cmp_lt_i32_e64 s[24:25], v2, v35
	s_and_saveexec_b64 s[0:1], s[24:25]
	s_cbranch_execz .LBB2_38
	ds_read_b32 v10, v8 offset:52800
	s_mov_b32 s3, 0x240000
	v_mov_b32_e32 v13, 0
	v_or3_b32 v12, v4, v2, s3
	s_waitcnt lgkmcnt(0)
	v_ashrrev_i32_e32 v11, 31, v10
	v_lshl_add_u64 v[10:11], v[12:13], 0, v[10:11]
	v_lshl_add_u64 v[12:13], v[10:11], 2, s[56:57]
	v_lshl_add_u64 v[10:11], v[10:11], 1, s[58:59]
	global_load_dword v20, v[12:13], off
	global_load_ushort v19, v[10:11], off
.LBB2_38:
	s_or_b64 exec, exec, s[0:1]
	v_mov_b32_e32 v15, 0
	v_mov_b32_e32 v18, 0
	v_mov_b32_e32 v17, 0
	s_waitcnt lgkmcnt(0)
	v_cmp_lt_i32_e64 s[22:23], v2, v33
	s_and_saveexec_b64 s[0:1], s[22:23]
	s_cbranch_execz .LBB2_40
	ds_read_b32 v10, v8 offset:52864
	s_mov_b32 s3, 0x280000
	v_mov_b32_e32 v13, 0
	v_or3_b32 v12, v4, v2, s3
	s_waitcnt lgkmcnt(0)
	v_ashrrev_i32_e32 v11, 31, v10
	v_lshl_add_u64 v[10:11], v[12:13], 0, v[10:11]
	v_lshl_add_u64 v[12:13], v[10:11], 2, s[56:57]
	v_lshl_add_u64 v[10:11], v[10:11], 1, s[58:59]
	global_load_dword v17, v[12:13], off
	global_load_ushort v18, v[10:11], off
.LBB2_40:
	s_or_b64 exec, exec, s[0:1]
	v_mov_b32_e32 v16, 0
	s_waitcnt lgkmcnt(0)
	v_cmp_lt_i32_e64 s[20:21], v2, v31
	s_and_saveexec_b64 s[0:1], s[20:21]
	s_cbranch_execz .LBB2_42
	ds_read_b32 v10, v8 offset:52928
	s_mov_b32 s3, 0x2c0000
	v_mov_b32_e32 v13, 0
	v_or3_b32 v12, v4, v2, s3
	s_waitcnt lgkmcnt(0)
	v_ashrrev_i32_e32 v11, 31, v10
	v_lshl_add_u64 v[10:11], v[12:13], 0, v[10:11]
	v_lshl_add_u64 v[12:13], v[10:11], 2, s[56:57]
	v_lshl_add_u64 v[10:11], v[10:11], 1, s[58:59]
	global_load_dword v16, v[12:13], off
	global_load_ushort v15, v[10:11], off
.LBB2_42:
	s_or_b64 exec, exec, s[0:1]
	v_mov_b32_e32 v11, 0
	v_mov_b32_e32 v14, 0
	v_mov_b32_e32 v13, 0
	s_waitcnt lgkmcnt(0)
	v_cmp_lt_i32_e64 s[18:19], v2, v55
	s_and_saveexec_b64 s[0:1], s[18:19]
	s_cbranch_execz .LBB2_44
	ds_read_b32 v12, v8 offset:52992
	s_mov_b32 s3, 0x300000
	v_mov_b32_e32 v5, 0
	v_or3_b32 v4, v4, v2, s3
	s_waitcnt lgkmcnt(0)
	v_ashrrev_i32_e32 v13, 31, v12
	v_lshl_add_u64 v[4:5], v[4:5], 0, v[12:13]
	v_lshl_add_u64 v[12:13], v[4:5], 2, s[56:57]
	v_lshl_add_u64 v[4:5], v[4:5], 1, s[58:59]
	global_load_dword v13, v[12:13], off
	s_nop 0
	global_load_ushort v14, v[4:5], off

	.amdhsa_kernel _Z12k_bucketsortPKjPKtPKiPiPj
		.amdhsa_group_segment_fixed_size 54144
		.amdhsa_private_segment_fixed_size 0
		.amdhsa_kernarg_size 40
		.amdhsa_user_sgpr_count 2
		.amdhsa_user_sgpr_dispatch_ptr 0
		.amdhsa_user_sgpr_queue_ptr 0
		.amdhsa_user_sgpr_kernarg_segment_ptr 1
		.amdhsa_user_sgpr_dispatch_id 0
		.amdhsa_user_sgpr_kernarg_preload_length 0
		.amdhsa_user_sgpr_kernarg_preload_offset 0
		.amdhsa_user_sgpr_private_segment_size 0
		.amdhsa_uses_dynamic_stack 0
		.amdhsa_enable_private_segment 0
		.amdhsa_system_sgpr_workgroup_id_x 1
		.amdhsa_system_sgpr_workgroup_id_y 0
		.amdhsa_system_sgpr_workgroup_id_z 0
		.amdhsa_system_sgpr_workgroup_info 0
		.amdhsa_system_vgpr_workitem_id 0
		.amdhsa_next_free_vgpr 64
		.amdhsa_next_free_sgpr 64
		.amdhsa_accum_offset 64
		.amdhsa_reserve_vcc 1
		.amdhsa_float_round_mode_32 0
		.amdhsa_float_round_mode_16_64 0
		.amdhsa_float_denorm_mode_32 3
		.amdhsa_float_denorm_mode_16_64 3
		.amdhsa_dx10_clamp 1
		.amdhsa_ieee_mode 1
		.amdhsa_fp16_overflow 0
		.amdhsa_tg_split 0
		.amdhsa_exception_fp_ieee_invalid_op 0
		.amdhsa_exception_fp_denorm_src 0
		.amdhsa_exception_fp_ieee_div_zero 0
		.amdhsa_exception_fp_ieee_overflow 0
		.amdhsa_exception_fp_ieee_underflow 0
		.amdhsa_exception_fp_ieee_inexact 0
		.amdhsa_exception_int_div_zero 0
	.end_amdhsa_kernel

amdhsa.kernels:
  - .agpr_count:     0
    .args:
      - .actual_access:  read_only
        .address_space:  global
        .offset:         0
        .size:           8
        .value_kind:     global_buffer
      - .actual_access:  read_only
        .address_space:  global
        .offset:         8
        .size:           8
        .value_kind:     global_buffer
      - .actual_access:  read_only
        .address_space:  global
        .offset:         16
        .size:           8
        .value_kind:     global_buffer
      - .actual_access:  read_only
        .address_space:  global
        .offset:         24
        .size:           8
        .value_kind:     global_buffer
      - .actual_access:  read_only
        .address_space:  global
        .offset:         32
        .size:           8
        .value_kind:     global_buffer
      - .actual_access:  read_only
        .address_space:  global
        .offset:         40
        .size:           8
        .value_kind:     global_buffer
      - .actual_access:  read_only
        .address_space:  global
        .offset:         48
        .size:           8
        .value_kind:     global_buffer
      - .actual_access:  read_only
        .address_space:  global
        .offset:         56
        .size:           8
        .value_kind:     global_buffer
      - .actual_access:  read_only
        .address_space:  global
        .offset:         64
        .size:           8
        .value_kind:     global_buffer
      - .actual_access:  read_only
        .address_space:  global
        .offset:         72
        .size:           8
        .value_kind:     global_buffer
      - .actual_access:  read_only
        .address_space:  global
        .offset:         80
        .size:           8
        .value_kind:     global_buffer
      - .actual_access:  read_only
        .address_space:  global
        .offset:         88
        .size:           8
        .value_kind:     global_buffer
      - .actual_access:  write_only
        .address_space:  global
        .offset:         96
        .size:           8
        .value_kind:     global_buffer
      - .actual_access:  write_only
        .address_space:  global
        .offset:         104
        .size:           8
        .value_kind:     global_buffer
      - .actual_access:  write_only
        .address_space:  global
        .offset:         112
        .size:           8
        .value_kind:     global_buffer
      - .actual_access:  write_only
        .address_space:  global
        .offset:         120
        .size:           8
        .value_kind:     global_buffer
      - .actual_access:  write_only
        .address_space:  global
        .offset:         128
        .size:           8
        .value_kind:     global_buffer
      - .actual_access:  write_only
        .address_space:  global
        .offset:         136
        .size:           8
        .value_kind:     global_buffer
      - .actual_access:  write_only
        .address_space:  global
        .offset:         144
        .size:           8
        .value_kind:     global_buffer
      - .actual_access:  write_only
        .address_space:  global
        .offset:         152
        .size:           8
        .value_kind:     global_buffer
      - .actual_access:  write_only
        .address_space:  global
        .offset:         160
        .size:           8
        .value_kind:     global_buffer
    .group_segment_fixed_size: 0
    .kernarg_segment_align: 8
    .kernarg_segment_size: 168
    .language:       OpenCL C
    .language_version:
      - 2
      - 0
    .max_flat_workgroup_size: 1024
    .name:           _Z6k_prepPKiS0_PKfS2_S2_S2_S2_S2_S2_S2_S2_S2_PDF16_S3_S3_PfS4_S4_PjS3_S5_
    .private_segment_fixed_size: 0
    .sgpr_count:     27
    .sgpr_spill_count: 0
    .symbol:         _Z6k_prepPKiS0_PKfS2_S2_S2_S2_S2_S2_S2_S2_S2_PDF16_S3_S3_PfS4_S4_PjS3_S5_.kd
    .uniform_work_group_size: 1
    .uses_dynamic_stack: false
    .vgpr_count:     61
    .vgpr_spill_count: 0
    .wavefront_size: 64
  - .agpr_count:     0
    .args:
      - .actual_access:  read_only
        .address_space:  global
        .offset:         0
        .size:           8
        .value_kind:     global_buffer
      - .actual_access:  read_only
        .address_space:  global
        .offset:         8
        .size:           8
        .value_kind:     global_buffer
      - .actual_access:  read_only
        .address_space:  global
        .offset:         16
        .size:           8
        .value_kind:     global_buffer
      - .actual_access:  write_only
        .address_space:  global
        .offset:         24
        .size:           8
        .value_kind:     global_buffer
      - .actual_access:  write_only
        .address_space:  global
        .offset:         32
        .size:           8
        .value_kind:     global_buffer
      - .actual_access:  write_only
        .address_space:  global
        .offset:         40
        .size:           8
        .value_kind:     global_buffer
      - .actual_access:  read_only
        .address_space:  global
        .offset:         48
        .size:           8
        .value_kind:     global_buffer
      - .actual_access:  read_only
        .address_space:  global
        .offset:         56
        .size:           8
        .value_kind:     global_buffer
      - .actual_access:  read_only
        .address_space:  global
        .offset:         64
        .size:           8
        .value_kind:     global_buffer
      - .actual_access:  read_only
        .address_space:  global
        .offset:         72
        .size:           8
        .value_kind:     global_buffer
      - .actual_access:  read_only
        .address_space:  global
        .offset:         80
        .size:           8
        .value_kind:     global_buffer
      - .actual_access:  read_only
        .address_space:  global
        .offset:         88
        .size:           8
        .value_kind:     global_buffer
      - .actual_access:  read_only
        .address_space:  global
        .offset:         96
        .size:           8
        .value_kind:     global_buffer
      - .actual_access:  read_only
        .address_space:  global
        .offset:         104
        .size:           8
        .value_kind:     global_buffer
      - .actual_access:  read_only
        .address_space:  global
        .offset:         112
        .size:           8
        .value_kind:     global_buffer
      - .actual_access:  read_only
        .address_space:  global
        .offset:         120
        .size:           8
        .value_kind:     global_buffer
      - .actual_access:  read_only
        .address_space:  global
        .offset:         128
        .size:           8
        .value_kind:     global_buffer
      - .actual_access:  write_only
        .address_space:  global
        .offset:         136
        .size:           8
        .value_kind:     global_buffer
      - .actual_access:  write_only
        .address_space:  global
        .offset:         144
        .size:           8
        .value_kind:     global_buffer
      - .actual_access:  write_only
        .address_space:  global
        .offset:         152
        .size:           8
        .value_kind:     global_buffer
      - .actual_access:  write_only
        .address_space:  global
        .offset:         160
        .size:           8
        .value_kind:     global_buffer
      - .actual_access:  write_only
        .address_space:  global
        .offset:         168
        .size:           8
        .value_kind:     global_buffer
    .group_segment_fixed_size: 1696
    .kernarg_segment_align: 8
    .kernarg_segment_size: 176
    .language:       OpenCL C
    .language_version:
      - 2
      - 0
    .max_flat_workgroup_size: 1024
    .name:           _Z11k_localsortPKiS0_S0_PjPtPiPKjPKfS7_S7_S7_S7_S7_S7_S7_S7_S7_PDF16_S8_S8_PfS9_
    .private_segment_fixed_size: 0
    .sgpr_count:     71
    .sgpr_spill_count: 0
    .symbol:         _Z11k_localsortPKiS0_S0_PjPtPiPKjPKfS7_S7_S7_S7_S7_S7_S7_S7_S7_PDF16_S8_S8_PfS9_.kd
    .uniform_work_group_size: 1
    .uses_dynamic_stack: false
    .vgpr_count:     95
    .vgpr_spill_count: 0
    .wavefront_size: 64
  - .agpr_count:     0
    .args:
      - .actual_access:  read_only
        .address_space:  global
        .offset:         0
        .size:           8
        .value_kind:     global_buffer
      - .actual_access:  read_only
        .address_space:  global
        .offset:         8
        .size:           8
        .value_kind:     global_buffer
      - .actual_access:  read_only
        .address_space:  global
        .offset:         16
        .size:           8
        .value_kind:     global_buffer
      - .actual_access:  write_only
        .address_space:  global
        .offset:         24
        .size:           8
        .value_kind:     global_buffer
      - .actual_access:  write_only
        .address_space:  global
        .offset:         32
        .size:           8
        .value_kind:     global_buffer
    .group_segment_fixed_size: 54144
    .kernarg_segment_align: 8
    .kernarg_segment_size: 40
    .language:       OpenCL C
    .language_version:
      - 2
      - 0
    .max_flat_workgroup_size: 1024
    .name:           _Z12k_bucketsortPKjPKtPKiPiPj
    .private_segment_fixed_size: 0
    .sgpr_count:     70
    .sgpr_spill_count: 0
    .symbol:         _Z12k_bucketsortPKjPKtPKiPiPj.kd
    .uniform_work_group_size: 1
    .uses_dynamic_stack: false
    .vgpr_count:     64
    .vgpr_spill_count: 0
    .wavefront_size: 64
  - .agpr_count:     0
    .args:
      - .actual_access:  read_only
        .address_space:  global
        .offset:         0
        .size:           8
        .value_kind:     global_buffer
      - .actual_access:  read_only
        .address_space:  global
        .offset:         8
        .size:           8
        .value_kind:     global_buffer
      - .actual_access:  write_only
        .address_space:  global
        .offset:         16
        .size:           8
        .value_kind:     global_buffer
    .group_segment_fixed_size: 0
    .kernarg_segment_align: 8
    .kernarg_segment_size: 24
    .language:       OpenCL C
    .language_version:
      - 2
      - 0
    .max_flat_workgroup_size: 256
    .name:           _Z7k_finalPKfS0_Pf
    .private_segment_fixed_size: 0
    .sgpr_count:     14
    .sgpr_spill_count: 0
    .symbol:         _Z7k_finalPKfS0_Pf.kd
    .uniform_work_group_size: 1
    .uses_dynamic_stack: false
    .vgpr_count:     10
    .vgpr_spill_count: 0
    .wavefront_size: 64
  - .agpr_count:     0
    .args:
      - .actual_access:  read_only
        .address_space:  global
        .offset:         0
        .size:           8
        .value_kind:     global_buffer
      - .actual_access:  read_only
        .address_space:  global
        .offset:         8
        .size:           8
        .value_kind:     global_buffer
      - .actual_access:  read_only
        .address_space:  global
        .offset:         16
        .size:           8
        .value_kind:     global_buffer
      - .actual_access:  read_only
        .address_space:  global
        .offset:         24
        .size:           8
        .value_kind:     global_buffer
      - .actual_access:  read_only
        .address_space:  global
        .offset:         32
        .size:           8
        .value_kind:     global_buffer
      - .actual_access:  read_only
        .address_space:  global
        .offset:         40
        .size:           8
        .value_kind:     global_buffer
      - .address_space:  global
        .offset:         48
        .size:           8
        .value_kind:     global_buffer
      - .actual_access:  write_only
        .address_space:  global
        .offset:         56
        .size:           8
        .value_kind:     global_buffer
      - .address_space:  global
        .offset:         64
        .size:           8
        .value_kind:     global_buffer
      - .actual_access:  read_only
        .address_space:  global
        .offset:         72
        .size:           8
        .value_kind:     global_buffer
      - .address_space:  global
        .offset:         80
        .size:           8
        .value_kind:     global_buffer
      - .actual_access:  read_only
        .address_space:  global
        .offset:         88
        .size:           8
        .value_kind:     global_buffer
      - .offset:         96
        .size:           4
        .value_kind:     hidden_block_count_x
      - .offset:         100
        .size:           4
        .value_kind:     hidden_block_count_y
      - .offset:         104
        .size:           4
        .value_kind:     hidden_block_count_z
      - .offset:         108
        .size:           2
        .value_kind:     hidden_group_size_x
      - .offset:         110
        .size:           2
        .value_kind:     hidden_group_size_y
      - .offset:         112
        .size:           2
        .value_kind:     hidden_group_size_z
      - .offset:         114
        .size:           2
        .value_kind:     hidden_remainder_x
      - .offset:         116
        .size:           2
        .value_kind:     hidden_remainder_y
      - .offset:         118
        .size:           2
        .value_kind:     hidden_remainder_z
      - .offset:         136
        .size:           8
        .value_kind:     hidden_global_offset_x
      - .offset:         144
        .size:           8
        .value_kind:     hidden_global_offset_y
      - .offset:         152
        .size:           8
        .value_kind:     hidden_global_offset_z
      - .offset:         160
        .size:           2
        .value_kind:     hidden_grid_dims
      - .offset:         216
        .size:           4
        .value_kind:     hidden_dynamic_lds_size
    .group_segment_fixed_size: 256
    .kernarg_segment_align: 8
    .kernarg_segment_size: 352
    .language:       OpenCL C
    .language_version:
      - 2
      - 0
    .max_flat_workgroup_size: 1024
    .name:           _Z7k_layerILi1EEvPKDF16_PKiPKjS3_S3_S1_PKfPDF16_PhS3_S7_Pf
    .private_segment_fixed_size: 0
    .sgpr_count:     38
    .sgpr_spill_count: 0
    .symbol:         _Z7k_layerILi1EEvPKDF16_PKiPKjS3_S3_S1_PKfPDF16_PhS3_S7_Pf.kd
    .uniform_work_group_size: 1
    .uses_dynamic_stack: false
    .vgpr_count:     114
    .vgpr_spill_count: 0
    .wavefront_size: 64
  - .agpr_count:     0
    .args:
      - .actual_access:  read_only
        .address_space:  global
        .offset:         0
        .size:           8
        .value_kind:     global_buffer
      - .actual_access:  read_only
        .address_space:  global
        .offset:         8
        .size:           8
        .value_kind:     global_buffer
      - .actual_access:  read_only
        .address_space:  global
        .offset:         16
        .size:           8
        .value_kind:     global_buffer
      - .actual_access:  read_only
        .address_space:  global
        .offset:         24
        .size:           8
        .value_kind:     global_buffer
      - .actual_access:  read_only
        .address_space:  global
        .offset:         32
        .size:           8
        .value_kind:     global_buffer
      - .actual_access:  read_only
        .address_space:  global
        .offset:         40
        .size:           8
        .value_kind:     global_buffer
      - .address_space:  global
        .offset:         48
        .size:           8
        .value_kind:     global_buffer
      - .actual_access:  read_only
        .address_space:  global
        .offset:         56
        .size:           8
        .value_kind:     global_buffer
      - .address_space:  global
        .offset:         64
        .size:           8
        .value_kind:     global_buffer
      - .actual_access:  read_only
        .address_space:  global
        .offset:         72
        .size:           8
        .value_kind:     global_buffer
      - .address_space:  global
        .offset:         80
        .size:           8
        .value_kind:     global_buffer
      - .address_space:  global
        .offset:         88
        .size:           8
        .value_kind:     global_buffer
      - .offset:         96
        .size:           4
        .value_kind:     hidden_block_count_x
      - .offset:         100
        .size:           4
        .value_kind:     hidden_block_count_y
      - .offset:         104
        .size:           4
        .value_kind:     hidden_block_count_z
      - .offset:         108
        .size:           2
        .value_kind:     hidden_group_size_x
      - .offset:         110
        .size:           2
        .value_kind:     hidden_group_size_y
      - .offset:         112
        .size:           2
        .value_kind:     hidden_group_size_z
      - .offset:         114
        .size:           2
        .value_kind:     hidden_remainder_x
      - .offset:         116
        .size:           2
        .value_kind:     hidden_remainder_y
      - .offset:         118
        .size:           2
        .value_kind:     hidden_remainder_z
      - .offset:         136
        .size:           8
        .value_kind:     hidden_global_offset_x
      - .offset:         144
        .size:           8
        .value_kind:     hidden_global_offset_y
      - .offset:         152
        .size:           8
        .value_kind:     hidden_global_offset_z
      - .offset:         160
        .size:           2
        .value_kind:     hidden_grid_dims
      - .offset:         216
        .size:           4
        .value_kind:     hidden_dynamic_lds_size
    .group_segment_fixed_size: 768
    .kernarg_segment_align: 8
    .kernarg_segment_size: 352
    .language:       OpenCL C
    .language_version:
      - 2
      - 0
    .max_flat_workgroup_size: 1024
    .name:           _Z7k_layerILi2EEvPKDF16_PKiPKjS3_S3_S1_PKfPDF16_PhS3_S7_Pf
    .private_segment_fixed_size: 0
    .sgpr_count:     44
    .sgpr_spill_count: 0
    .symbol:         _Z7k_layerILi2EEvPKDF16_PKiPKjS3_S3_S1_PKfPDF16_PhS3_S7_Pf.kd
    .uniform_work_group_size: 1
    .uses_dynamic_stack: false
    .vgpr_count:     102
    .vgpr_spill_count: 0
    .wavefront_size: 64
